# gate|up GEMM: non-scaled v_mfma_f32_16x16x128_f8f6f4 instead of the block-scale form; the exact 2^-5 accumulator scale applied once per unit at the head of the SwiGLU epilogue
# baseline (speedup 1.0000x reference)
; #define PG8_STAGE(bufoff, gbase, voff) do { _Pragma("unroll") for (int _i = 0; _i < 2; ++_i) \
;         __builtin_amdgcn_global_load_lds((const unsigned*)((const char*)(gbase) + (voff)[_i]), (LAS unsigned*)(lds + (bufoff) + ldsw + _i * 8192), 16, 0, 0); } while (0)
; #define PG8_LDA(dst, b, h) do { _Pragma("unroll") for (int m = 0; m < 4; ++m) _Pragma("unroll") for (int k = 0; k < 2; ++k) dst[m][k] = *(const LAS bf16x8*)(lds + PG8_SA(b, h) + aoff + m * 2048 + k * KOFF); } while (0)
; #define PG8_LDB(dst, b, h) do { _Pragma("unroll") for (int n = 0; n < 2; ++n) _Pragma("unroll") for (int k = 0; k < 2; ++k) dst[n][k] = *(const LAS bf16x8*)(lds + PG8_SB(b, h) + boff + n * 2048 + k * KOFF); } while (0)
; #define PG8_WAIT_V(n) asm volatile("s_waitcnt vmcnt(" #n ")" ::: "memory")
; #define PG8_WAIT_L(n) asm volatile("s_waitcnt lgkmcnt(" #n ")" ::: "memory")
; #define PG8_BAR __builtin_amdgcn_s_barrier()
; #define PG8_SCHED __builtin_amdgcn_sched_barrier(0)
; #define PG8_AOFF(u_, o0, o1) do { _Pragma("unroll") for (int _i = 0; _i < 2; ++_i) { const int r0 = (u_).pm * BM + Rr[_i], r1 = r0 + HALF; \
;         const int g0 = GATHER ? g.rowidx[r0] : r0, g1 = GATHER ? g.rowidx[r1] : r1; \
;         o0[_i] = (unsigned)g0 * (unsigned)K + (unsigned)Cc[_i]; o1[_i] = (unsigned)g1 * (unsigned)K + (unsigned)Cc[_i]; } } while (0)
; template <class Epi, class Sched, bool GATHER, bool FP8 = false, bool ALIGN = true>
; __device__ __forceinline__ void gemm_phase(LAS unsigned char* lds, int wave, const Gemm g, const Sched& S, const Epi& E) {
;     ...
;             PG8_LDB(B0, 0, 0); PG8_LDB(B1, 0, 1); PG8_SCHED; PG8_LDA(At, 0, 0); PG8_STAGE(PG8_SA(1, 1), a1, ca1);
;             if (last && has_next) PG8_AOFF(nxt, ca0, ca1);
;             PG8_WAIT_V(8); PG8_WAIT_L(0); PG8_BAR; PG8_MMA(0, 0, At, B0); PG8_MMA(0, 1, At, B1); PG8_BAR; PG8_SCHED;
;             PG8_LDA(At, 0, 1); PG8_STAGE(PG8_SB(0, 0), b2, voffB0); PG8_STAGE(PG8_SB(0, 1), b2, voffB1); PG8_STAGE(PG8_SA(0, 0), a2, ca0);
;             PG8_WAIT_V(8); PG8_WAIT_L(0); PG8_BAR; PG8_MMA(1, 0, At, B0); PG8_MMA(1, 1, At, B1); PG8_BAR; PG8_SCHED;
;             PG8_LDB(B0, 1, 0); PG8_LDB(B1, 1, 1); PG8_SCHED; PG8_LDA(At, 1, 0); PG8_STAGE(PG8_SA(0, 1), a2, ca1);
.Lgu_norow:
	s_setprio 1
	s_waitcnt lgkmcnt(0)
	v_mfma_f32_16x16x128_f8f6f4 v[188:191], v[16:23], v[56:63], 0
	v_mfma_f32_16x16x128_f8f6f4 v[180:183], v[24:31], v[56:63], 0
	v_mfma_f32_16x16x128_f8f6f4 v[172:175], v[16:23], v[48:55], 0
	v_mfma_f32_16x16x128_f8f6f4 v[164:167], v[24:31], v[48:55], 0
	v_mfma_f32_16x16x128_f8f6f4 v[156:159], v[16:23], v[40:47], 0
	v_mfma_f32_16x16x128_f8f6f4 v[148:151], v[24:31], v[40:47], 0
	v_mfma_f32_16x16x128_f8f6f4 v[140:143], v[16:23], v[32:39], 0
	v_mfma_f32_16x16x128_f8f6f4 v[132:135], v[24:31], v[32:39], 0
	s_setprio 0
	s_setprio 1
	v_mfma_f32_16x16x128_f8f6f4 v[184:187], v[0:7], v[56:63], 0
	v_mfma_f32_16x16x128_f8f6f4 v[176:179], v[8:15], v[56:63], 0
	v_mfma_f32_16x16x128_f8f6f4 v[168:171], v[0:7], v[48:55], 0
	v_mfma_f32_16x16x128_f8f6f4 v[160:163], v[8:15], v[48:55], 0
	v_mfma_f32_16x16x128_f8f6f4 v[152:155], v[0:7], v[40:47], 0
	v_mfma_f32_16x16x128_f8f6f4 v[144:147], v[8:15], v[40:47], 0
	v_mfma_f32_16x16x128_f8f6f4 v[136:139], v[0:7], v[32:39], 0
	v_mfma_f32_16x16x128_f8f6f4 v[128:131], v[8:15], v[32:39], 0
	s_setprio 0
	s_barrier
	s_mov_b32 m0, s34
	v_lshl_add_u64 v[196:197], s[14:15], 0, v[204:205]
	ds_read_b128 v[32:35], v238 offset:16384
	ds_read_b128 v[36:39], v238 offset:17408
	ds_read_b128 v[40:43], v238 offset:18432
	ds_read_b128 v[44:47], v238 offset:19456
	ds_read_b128 v[48:51], v238 offset:20480
	ds_read_b128 v[52:55], v238 offset:21504
	ds_read_b128 v[56:59], v238 offset:22528
	ds_read_b128 v[60:63], v238 offset:23552
	global_load_lds_dwordx4 v[196:197], off
	v_lshl_add_u64 v[198:199], s[14:15], 0, v[208:209]
	s_mov_b32 m0, s35
	v_lshl_add_u64 v[200:201], s[14:15], 0, v[206:207]
	global_load_lds_dwordx4 v[198:199], off
	s_mov_b32 m0, s40
	v_lshl_add_u64 v[202:203], s[14:15], 0, v[210:211]
	global_load_lds_dwordx4 v[200:201], off
	s_mov_b32 m0, s41
	v_mov_b32_e32 v215, v193
	global_load_lds_dwordx4 v[202:203], off
	s_mov_b32 m0, s31
	v_lshl_add_u64 v[226:227], s[12:13], 0, v[192:193]
	global_load_lds_dwordx4 v192, s[12:13]
	s_mov_b32 m0, s53
	v_lshl_add_u64 v[228:229], s[12:13], 0, v[214:215]
	global_load_lds_dwordx4 v214, s[12:13]
	s_waitcnt vmcnt(8)
	s_waitcnt lgkmcnt(0)
	s_barrier
	s_setprio 1
	s_waitcnt lgkmcnt(0)
	v_mfma_f32_16x16x128_f8f6f4 v[124:127], v[16:23], v[32:39], 0
	v_mfma_f32_16x16x128_f8f6f4 v[116:119], v[24:31], v[32:39], 0
	v_mfma_f32_16x16x128_f8f6f4 v[108:111], v[16:23], v[40:47], 0
	v_mfma_f32_16x16x128_f8f6f4 v[100:103], v[24:31], v[40:47], 0
	v_mfma_f32_16x16x128_f8f6f4 v[92:95], v[16:23], v[48:55], 0
	v_mfma_f32_16x16x128_f8f6f4 v[84:87], v[24:31], v[48:55], 0
	v_mfma_f32_16x16x128_f8f6f4 v[76:79], v[16:23], v[56:63], 0
	v_mfma_f32_16x16x128_f8f6f4 v[68:71], v[24:31], v[56:63], 0
	s_setprio 0
	s_setprio 1
	v_mfma_f32_16x16x128_f8f6f4 v[120:123], v[0:7], v[32:39], 0
	v_mfma_f32_16x16x128_f8f6f4 v[112:115], v[8:15], v[32:39], 0
	v_mfma_f32_16x16x128_f8f6f4 v[104:107], v[0:7], v[40:47], 0
	v_mfma_f32_16x16x128_f8f6f4 v[96:99], v[8:15], v[40:47], 0
	v_mfma_f32_16x16x128_f8f6f4 v[88:91], v[0:7], v[48:55], 0
	v_mfma_f32_16x16x128_f8f6f4 v[80:83], v[8:15], v[48:55], 0
	v_mfma_f32_16x16x128_f8f6f4 v[72:75], v[0:7], v[56:63], 0
	v_mfma_f32_16x16x128_f8f6f4 v[64:67], v[8:15], v[56:63], 0
	s_setprio 0
	s_barrier
	s_add_i32 s14, 0, 0x18000
	s_add_i32 s15, 0, 0x1c000
	v_add_u32_e32 v12, s14, v236
	v_add_u32_e32 v28, s15, v236
	ds_read_b128 v[0:3], v12
	ds_read_b128 v[4:7], v12 offset:1024
	ds_read_b128 v[8:11], v12 offset:2048
	ds_read_b128 v[12:15], v12 offset:3072
	ds_read_b128 v[16:19], v28
	ds_read_b128 v[20:23], v28 offset:1024
	ds_read_b128 v[24:27], v28 offset:2048
	ds_read_b128 v[28:31], v28 offset:3072
	s_mov_b32 m0, s56
	v_lshl_add_u64 v[230:231], s[12:13], 0, v[212:213]
	ds_read_b128 v[32:35], v238 offset:32768
	ds_read_b128 v[36:39], v238 offset:33792
	ds_read_b128 v[40:43], v238 offset:34816
	ds_read_b128 v[44:47], v238 offset:35840
	ds_read_b128 v[48:51], v238 offset:36864
	ds_read_b128 v[52:55], v238 offset:37888
	ds_read_b128 v[56:59], v238 offset:38912
	ds_read_b128 v[60:63], v238 offset:39936
	global_load_lds_dwordx4 v[230:231], off
	v_lshl_add_u64 v[230:231], s[12:13], 0, v[216:217]
	s_mov_b32 m0, s57
	s_nop 0
	global_load_lds_dwordx4 v[230:231], off
	s_waitcnt vmcnt(8)
	s_waitcnt lgkmcnt(0)
	s_barrier
; #define PG8_STAGE(bufoff, gbase, voff) do { _Pragma("unroll") for (int _i = 0; _i < 2; ++_i) \
;         __builtin_amdgcn_global_load_lds((const unsigned*)((const char*)(gbase) + (voff)[_i]), (LAS unsigned*)(lds + (bufoff) + ldsw + _i * 8192), 16, 0, 0); } while (0)
; #define PG8_LDA(dst, b, h) do { _Pragma("unroll") for (int m = 0; m < 4; ++m) _Pragma("unroll") for (int k = 0; k < 2; ++k) dst[m][k] = *(const LAS bf16x8*)(lds + PG8_SA(b, h) + aoff + m * 2048 + k * KOFF); } while (0)
; #define PG8_LDB(dst, b, h) do { _Pragma("unroll") for (int n = 0; n < 2; ++n) _Pragma("unroll") for (int k = 0; k < 2; ++k) dst[n][k] = *(const LAS bf16x8*)(lds + PG8_SB(b, h) + boff + n * 2048 + k * KOFF); } while (0)
; #define PG8_WAIT_V(n) asm volatile("s_waitcnt vmcnt(" #n ")" ::: "memory")
; #define PG8_WAIT_L(n) asm volatile("s_waitcnt lgkmcnt(" #n ")" ::: "memory")
; #define PG8_BAR __builtin_amdgcn_s_barrier()
; #define PG8_SCHED __builtin_amdgcn_sched_barrier(0)
; template <class Epi, class Sched, bool GATHER, bool FP8 = false, bool ALIGN = true>
; __device__ __forceinline__ void gemm_phase(LAS unsigned char* lds, int wave, const Gemm g, const Sched& S, const Epi& E) {
;     ...
;             PG8_LDB(B0, 1, 0); PG8_LDB(B1, 1, 1); PG8_SCHED; PG8_LDA(At, 1, 0); PG8_STAGE(PG8_SA(0, 1), a2, ca1);
;             PG8_WAIT_V(8); PG8_WAIT_L(0); PG8_BAR; PG8_MMA(0, 0, At, B0); PG8_MMA(0, 1, At, B1); PG8_BAR; PG8_SCHED;
;             PG8_LDA(At, 1, 1); PG8_STAGE(PG8_SB(1, 0), b3, voffB0); PG8_STAGE(PG8_SB(1, 1), b3, voffB1); PG8_STAGE(PG8_SA(1, 0), a3, ca0);
;             PG8_WAIT_V(8); PG8_WAIT_L(0); PG8_BAR; PG8_MMA(1, 0, At, B0); PG8_MMA(1, 1, At, B1); PG8_BAR; PG8_SCHED;
;         }
	s_setprio 1
	s_waitcnt lgkmcnt(0)
	v_mfma_f32_16x16x128_f8f6f4 v[188:191], v[0:7], v[32:39], v[188:191]
	v_mfma_f32_16x16x128_f8f6f4 v[180:183], v[8:15], v[32:39], v[180:183]
	v_mfma_f32_16x16x128_f8f6f4 v[172:175], v[0:7], v[40:47], v[172:175]
	v_mfma_f32_16x16x128_f8f6f4 v[164:167], v[8:15], v[40:47], v[164:167]
	v_mfma_f32_16x16x128_f8f6f4 v[156:159], v[0:7], v[48:55], v[156:159]
	v_mfma_f32_16x16x128_f8f6f4 v[148:151], v[8:15], v[48:55], v[148:151]
	v_mfma_f32_16x16x128_f8f6f4 v[140:143], v[0:7], v[56:63], v[140:143]
	v_mfma_f32_16x16x128_f8f6f4 v[132:135], v[8:15], v[56:63], v[132:135]
	s_setprio 0
	s_setprio 1
	v_mfma_f32_16x16x128_f8f6f4 v[184:187], v[16:23], v[32:39], v[184:187]
	v_mfma_f32_16x16x128_f8f6f4 v[176:179], v[24:31], v[32:39], v[176:179]
	v_mfma_f32_16x16x128_f8f6f4 v[168:171], v[16:23], v[40:47], v[168:171]
	v_mfma_f32_16x16x128_f8f6f4 v[160:163], v[24:31], v[40:47], v[160:163]
	v_mfma_f32_16x16x128_f8f6f4 v[152:155], v[16:23], v[48:55], v[152:155]
	v_mfma_f32_16x16x128_f8f6f4 v[144:147], v[24:31], v[48:55], v[144:147]
	v_mfma_f32_16x16x128_f8f6f4 v[136:139], v[16:23], v[56:63], v[136:139]
	v_mfma_f32_16x16x128_f8f6f4 v[128:131], v[24:31], v[56:63], v[128:131]
	s_setprio 0
	s_barrier
	s_add_i32 s12, s14, s30
	v_lshl_add_u64 v[196:197], v[196:197], 0, s[62:63]
	s_mov_b32 m0, s12
	ds_read_b128 v[32:35], v238 offset:49152
	ds_read_b128 v[36:39], v238 offset:50176
	ds_read_b128 v[40:43], v238 offset:51200
	ds_read_b128 v[44:47], v238 offset:52224
	ds_read_b128 v[48:51], v238 offset:53248
	ds_read_b128 v[52:55], v238 offset:54272
	ds_read_b128 v[56:59], v238 offset:55296
	ds_read_b128 v[60:63], v238 offset:56320
	global_load_lds_dwordx4 v[196:197], off
	v_lshl_add_u64 v[196:197], v[198:199], 0, s[62:63]
	s_add_i32 m0, s12, 0x2000
	s_add_i32 s12, s15, s30
	global_load_lds_dwordx4 v[196:197], off
	v_lshl_add_u64 v[196:197], v[200:201], 0, s[62:63]
	s_mov_b32 m0, s12
	s_nop 0
	global_load_lds_dwordx4 v[196:197], off
	v_lshl_add_u64 v[196:197], v[202:203], 0, s[62:63]
	s_add_i32 m0, s12, 0x2000
	s_nop 0
	global_load_lds_dwordx4 v[196:197], off
	v_lshl_add_u64 v[196:197], v[226:227], 0, s[62:63]
	s_mov_b32 m0, s58
	s_nop 0
	global_load_lds_dwordx4 v[196:197], off
	v_lshl_add_u64 v[196:197], v[228:229], 0, s[62:63]
	s_mov_b32 m0, s59
	s_nop 0
	global_load_lds_dwordx4 v[196:197], off
	s_waitcnt vmcnt(8)
	s_waitcnt lgkmcnt(0)
	s_barrier
	s_setprio 1
	s_waitcnt lgkmcnt(0)
	v_mfma_f32_16x16x128_f8f6f4 v[124:127], v[0:7], v[32:39], v[124:127]
	v_mfma_f32_16x16x128_f8f6f4 v[116:119], v[8:15], v[32:39], v[116:119]
	v_mfma_f32_16x16x128_f8f6f4 v[108:111], v[0:7], v[40:47], v[108:111]
	v_mfma_f32_16x16x128_f8f6f4 v[100:103], v[8:15], v[40:47], v[100:103]
	v_mfma_f32_16x16x128_f8f6f4 v[92:95], v[0:7], v[48:55], v[92:95]
	v_mfma_f32_16x16x128_f8f6f4 v[84:87], v[8:15], v[48:55], v[84:87]
	v_mfma_f32_16x16x128_f8f6f4 v[76:79], v[0:7], v[56:63], v[76:79]
	v_mfma_f32_16x16x128_f8f6f4 v[68:71], v[8:15], v[56:63], v[68:71]
	s_setprio 0
	s_setprio 1
	v_mfma_f32_16x16x128_f8f6f4 v[120:123], v[16:23], v[32:39], v[120:123]
	v_mfma_f32_16x16x128_f8f6f4 v[112:115], v[24:31], v[32:39], v[112:115]
	v_mfma_f32_16x16x128_f8f6f4 v[104:107], v[16:23], v[40:47], v[104:107]
	v_mfma_f32_16x16x128_f8f6f4 v[96:99], v[24:31], v[40:47], v[96:99]
	v_mfma_f32_16x16x128_f8f6f4 v[88:91], v[16:23], v[48:55], v[88:91]
	v_mfma_f32_16x16x128_f8f6f4 v[80:83], v[24:31], v[48:55], v[80:83]
	v_mfma_f32_16x16x128_f8f6f4 v[72:75], v[16:23], v[56:63], v[72:75]
	v_mfma_f32_16x16x128_f8f6f4 v[64:67], v[24:31], v[56:63], v[64:67]
	s_setprio 0
	s_barrier
	s_add_i32 s83, s83, 2
	s_add_u32 s10, s10, 0x100
	s_addc_u32 s11, s11, 0
	s_add_u32 s49, s49, 0x100
	s_addc_u32 s82, s82, 0
	s_cmp_gt_u32 s83, 13
	s_cbranch_scc1 .LBB0_1083
	s_branch .LBB0_1081

; #define PG8_STAGE(bufoff, gbase, voff) do { _Pragma("unroll") for (int _i = 0; _i < 2; ++_i) \
;         __builtin_amdgcn_global_load_lds((const unsigned*)((const char*)(gbase) + (voff)[_i]), (LAS unsigned*)(lds + (bufoff) + ldsw + _i * 8192), 16, 0, 0); } while (0)
; #define PG8_LDA(dst, b, h) do { _Pragma("unroll") for (int m = 0; m < 4; ++m) _Pragma("unroll") for (int k = 0; k < 2; ++k) dst[m][k] = *(const LAS bf16x8*)(lds + PG8_SA(b, h) + aoff + m * 2048 + k * KOFF); } while (0)
; #define PG8_LDB(dst, b, h) do { _Pragma("unroll") for (int n = 0; n < 2; ++n) _Pragma("unroll") for (int k = 0; k < 2; ++k) dst[n][k] = *(const LAS bf16x8*)(lds + PG8_SB(b, h) + boff + n * 2048 + k * KOFF); } while (0)
; #define PG8_WAIT_V(n) asm volatile("s_waitcnt vmcnt(" #n ")" ::: "memory")
; #define PG8_WAIT_L(n) asm volatile("s_waitcnt lgkmcnt(" #n ")" ::: "memory")
; #define PG8_BAR __builtin_amdgcn_s_barrier()
; #define PG8_SCHED __builtin_amdgcn_sched_barrier(0)
; template <class Epi, class Sched, bool GATHER, bool FP8 = false, bool ALIGN = true>
; __device__ __forceinline__ void gemm_phase(LAS unsigned char* lds, int wave, const Gemm g, const Sched& S, const Epi& E) {
;     ...
;         for (int t = 0; t < nt; t += 2) {
;             const bool last = (t == nt - 2);
;             const char* a1 = Ab + (size_t)(t + 1) * kstep;
;             const char* a2 = last ? Ab : Ab + (size_t)(t + 2) * kstep; const char* b2 = last ? nB : cB + (size_t)(t + 2) * kstep;
;             const char* a3 = a2 + kstep; const char* b3 = b2 + kstep;
;             PG8_LDB(B0, 0, 0); PG8_LDB(B1, 0, 1); PG8_SCHED; PG8_LDA(At, 0, 0); PG8_STAGE(PG8_SA(1, 1), a1, ca1);
;             if (last && has_next) PG8_AOFF(nxt, ca0, ca1);
;             PG8_WAIT_V(8); PG8_WAIT_L(0); PG8_BAR; PG8_MMA(0, 0, At, B0); PG8_MMA(0, 1, At, B1); PG8_BAR; PG8_SCHED;
;             PG8_LDA(At, 0, 1); PG8_STAGE(PG8_SB(0, 0), b2, voffB0); PG8_STAGE(PG8_SB(0, 1), b2, voffB1); PG8_STAGE(PG8_SA(0, 0), a2, ca0);
;             PG8_WAIT_V(8); PG8_WAIT_L(0); PG8_BAR; PG8_MMA(1, 0, At, B0); PG8_MMA(1, 1, At, B1); PG8_BAR; PG8_SCHED;
.LBB0_1080:
	s_waitcnt vmcnt(8)
	s_add_u32 s14, s10, 0x80
	s_waitcnt lgkmcnt(0)
	s_addc_u32 s15, s11, 0
	s_and_b64 s[12:13], s[12:13], exec
	v_mov_b32_e32 v217, v193
	s_cselect_b32 s13, s7, s15
	s_cselect_b32 s12, s6, s14
	s_cselect_b32 s15, s5, s82
	s_cselect_b32 s14, s9, s49
	s_barrier
	s_setprio 1
	s_waitcnt lgkmcnt(0)
	v_mfma_f32_16x16x128_f8f6f4 v[188:191], v[16:23], v[56:63], v[188:191]
	v_mfma_f32_16x16x128_f8f6f4 v[180:183], v[24:31], v[56:63], v[180:183]
	v_mfma_f32_16x16x128_f8f6f4 v[172:175], v[16:23], v[48:55], v[172:175]
	v_mfma_f32_16x16x128_f8f6f4 v[164:167], v[24:31], v[48:55], v[164:167]
	v_mfma_f32_16x16x128_f8f6f4 v[156:159], v[16:23], v[40:47], v[156:159]
	v_mfma_f32_16x16x128_f8f6f4 v[148:151], v[24:31], v[40:47], v[148:151]
	v_mfma_f32_16x16x128_f8f6f4 v[140:143], v[16:23], v[32:39], v[140:143]
	v_mfma_f32_16x16x128_f8f6f4 v[132:135], v[24:31], v[32:39], v[132:135]
	s_setprio 0
	s_setprio 1
	v_mfma_f32_16x16x128_f8f6f4 v[184:187], v[0:7], v[56:63], v[184:187]
	v_mfma_f32_16x16x128_f8f6f4 v[176:179], v[8:15], v[56:63], v[176:179]
	v_mfma_f32_16x16x128_f8f6f4 v[168:171], v[0:7], v[48:55], v[168:171]
	v_mfma_f32_16x16x128_f8f6f4 v[160:163], v[8:15], v[48:55], v[160:163]
	v_mfma_f32_16x16x128_f8f6f4 v[152:155], v[0:7], v[40:47], v[152:155]
	v_mfma_f32_16x16x128_f8f6f4 v[144:147], v[8:15], v[40:47], v[144:147]
	v_mfma_f32_16x16x128_f8f6f4 v[136:139], v[0:7], v[32:39], v[136:139]
	v_mfma_f32_16x16x128_f8f6f4 v[128:131], v[8:15], v[32:39], v[128:131]
	s_setprio 0
	s_barrier
	s_mov_b32 m0, s34
	v_lshl_add_u64 v[196:197], s[14:15], 0, v[204:205]
	ds_read_b128 v[32:35], v238 offset:16384
	ds_read_b128 v[36:39], v238 offset:17408
	ds_read_b128 v[40:43], v238 offset:18432
	ds_read_b128 v[44:47], v238 offset:19456
	ds_read_b128 v[48:51], v238 offset:20480
	ds_read_b128 v[52:55], v238 offset:21504
	ds_read_b128 v[56:59], v238 offset:22528
	ds_read_b128 v[60:63], v238 offset:23552
	global_load_lds_dwordx4 v[196:197], off
	v_lshl_add_u64 v[198:199], s[14:15], 0, v[208:209]
	s_mov_b32 m0, s35
	v_lshl_add_u64 v[200:201], s[14:15], 0, v[206:207]
	global_load_lds_dwordx4 v[198:199], off
	s_mov_b32 m0, s40
	v_lshl_add_u64 v[202:203], s[14:15], 0, v[210:211]
	global_load_lds_dwordx4 v[200:201], off
	s_mov_b32 m0, s41
	v_mov_b32_e32 v215, v193
	global_load_lds_dwordx4 v[202:203], off
	s_mov_b32 m0, s31
	v_lshl_add_u64 v[226:227], s[12:13], 0, v[192:193]
	global_load_lds_dwordx4 v192, s[12:13]
	s_mov_b32 m0, s53
	v_lshl_add_u64 v[228:229], s[12:13], 0, v[214:215]
	global_load_lds_dwordx4 v214, s[12:13]
	s_waitcnt vmcnt(8)
	s_waitcnt lgkmcnt(0)
	s_barrier
	s_setprio 1
	s_waitcnt lgkmcnt(0)
	v_mfma_f32_16x16x128_f8f6f4 v[124:127], v[16:23], v[32:39], v[124:127]
	v_mfma_f32_16x16x128_f8f6f4 v[116:119], v[24:31], v[32:39], v[116:119]
	v_mfma_f32_16x16x128_f8f6f4 v[108:111], v[16:23], v[40:47], v[108:111]
	v_mfma_f32_16x16x128_f8f6f4 v[100:103], v[24:31], v[40:47], v[100:103]
	v_mfma_f32_16x16x128_f8f6f4 v[92:95], v[16:23], v[48:55], v[92:95]
	v_mfma_f32_16x16x128_f8f6f4 v[84:87], v[24:31], v[48:55], v[84:87]
	v_mfma_f32_16x16x128_f8f6f4 v[76:79], v[16:23], v[56:63], v[76:79]
	v_mfma_f32_16x16x128_f8f6f4 v[68:71], v[24:31], v[56:63], v[68:71]
	s_setprio 0
	s_setprio 1
	v_mfma_f32_16x16x128_f8f6f4 v[120:123], v[0:7], v[32:39], v[120:123]
	v_mfma_f32_16x16x128_f8f6f4 v[112:115], v[8:15], v[32:39], v[112:115]
	v_mfma_f32_16x16x128_f8f6f4 v[104:107], v[0:7], v[40:47], v[104:107]
	v_mfma_f32_16x16x128_f8f6f4 v[96:99], v[8:15], v[40:47], v[96:99]
	v_mfma_f32_16x16x128_f8f6f4 v[88:91], v[0:7], v[48:55], v[88:91]
	v_mfma_f32_16x16x128_f8f6f4 v[80:83], v[8:15], v[48:55], v[80:83]
	v_mfma_f32_16x16x128_f8f6f4 v[72:75], v[0:7], v[56:63], v[72:75]
	v_mfma_f32_16x16x128_f8f6f4 v[64:67], v[8:15], v[56:63], v[64:67]
	s_setprio 0
	s_barrier
; #define PG8_STAGE(bufoff, gbase, voff) do { _Pragma("unroll") for (int _i = 0; _i < 2; ++_i) \
;         __builtin_amdgcn_global_load_lds((const unsigned*)((const char*)(gbase) + (voff)[_i]), (LAS unsigned*)(lds + (bufoff) + ldsw + _i * 8192), 16, 0, 0); } while (0)
; #define PG8_LDA(dst, b, h) do { _Pragma("unroll") for (int m = 0; m < 4; ++m) _Pragma("unroll") for (int k = 0; k < 2; ++k) dst[m][k] = *(const LAS bf16x8*)(lds + PG8_SA(b, h) + aoff + m * 2048 + k * KOFF); } while (0)
; #define PG8_LDB(dst, b, h) do { _Pragma("unroll") for (int n = 0; n < 2; ++n) _Pragma("unroll") for (int k = 0; k < 2; ++k) dst[n][k] = *(const LAS bf16x8*)(lds + PG8_SB(b, h) + boff + n * 2048 + k * KOFF); } while (0)
; #define PG8_WAIT_V(n) asm volatile("s_waitcnt vmcnt(" #n ")" ::: "memory")
; #define PG8_WAIT_L(n) asm volatile("s_waitcnt lgkmcnt(" #n ")" ::: "memory")
; #define PG8_BAR __builtin_amdgcn_s_barrier()
; #define PG8_SCHED __builtin_amdgcn_sched_barrier(0)
; template <class Epi, class Sched, bool GATHER, bool FP8 = false, bool ALIGN = true>
; __device__ __forceinline__ void gemm_phase(LAS unsigned char* lds, int wave, const Gemm g, const Sched& S, const Epi& E) {
;     ...
;             PG8_LDB(B0, 1, 0); PG8_LDB(B1, 1, 1); PG8_SCHED; PG8_LDA(At, 1, 0); PG8_STAGE(PG8_SA(0, 1), a2, ca1);
;             PG8_WAIT_V(8); PG8_WAIT_L(0); PG8_BAR; PG8_MMA(0, 0, At, B0); PG8_MMA(0, 1, At, B1); PG8_BAR; PG8_SCHED;
;             PG8_LDA(At, 1, 1); PG8_STAGE(PG8_SB(1, 0), b3, voffB0); PG8_STAGE(PG8_SB(1, 1), b3, voffB1); PG8_STAGE(PG8_SA(1, 0), a3, ca0);
;             PG8_WAIT_V(8); PG8_WAIT_L(0); PG8_BAR; PG8_MMA(1, 0, At, B0); PG8_MMA(1, 1, At, B1); PG8_BAR; PG8_SCHED;
;         }
	s_add_i32 s14, 0, 0x18000
	s_add_i32 s15, 0, 0x1c000
	v_add_u32_e32 v12, s14, v236
	v_add_u32_e32 v28, s15, v236
	ds_read_b128 v[0:3], v12
	ds_read_b128 v[4:7], v12 offset:1024
	ds_read_b128 v[8:11], v12 offset:2048
	ds_read_b128 v[12:15], v12 offset:3072
	ds_read_b128 v[16:19], v28
	ds_read_b128 v[20:23], v28 offset:1024
	ds_read_b128 v[24:27], v28 offset:2048
	ds_read_b128 v[28:31], v28 offset:3072
	s_mov_b32 m0, s56
	v_lshl_add_u64 v[230:231], s[12:13], 0, v[212:213]
	ds_read_b128 v[32:35], v238 offset:32768
	ds_read_b128 v[36:39], v238 offset:33792
	ds_read_b128 v[40:43], v238 offset:34816
	ds_read_b128 v[44:47], v238 offset:35840
	ds_read_b128 v[48:51], v238 offset:36864
	ds_read_b128 v[52:55], v238 offset:37888
	ds_read_b128 v[56:59], v238 offset:38912
	ds_read_b128 v[60:63], v238 offset:39936
	global_load_lds_dwordx4 v[230:231], off
	v_lshl_add_u64 v[230:231], s[12:13], 0, v[216:217]
	s_mov_b32 m0, s57
	s_nop 0
	global_load_lds_dwordx4 v[230:231], off
	s_waitcnt vmcnt(8)
	s_waitcnt lgkmcnt(0)
	s_barrier
	s_setprio 1
	s_waitcnt lgkmcnt(0)
	v_mfma_f32_16x16x128_f8f6f4 v[188:191], v[0:7], v[32:39], v[188:191]
	v_mfma_f32_16x16x128_f8f6f4 v[180:183], v[8:15], v[32:39], v[180:183]
	v_mfma_f32_16x16x128_f8f6f4 v[172:175], v[0:7], v[40:47], v[172:175]
	v_mfma_f32_16x16x128_f8f6f4 v[164:167], v[8:15], v[40:47], v[164:167]
	v_mfma_f32_16x16x128_f8f6f4 v[156:159], v[0:7], v[48:55], v[156:159]
	v_mfma_f32_16x16x128_f8f6f4 v[148:151], v[8:15], v[48:55], v[148:151]
	v_mfma_f32_16x16x128_f8f6f4 v[140:143], v[0:7], v[56:63], v[140:143]
	v_mfma_f32_16x16x128_f8f6f4 v[132:135], v[8:15], v[56:63], v[132:135]
	s_setprio 0
	s_setprio 1
	v_mfma_f32_16x16x128_f8f6f4 v[184:187], v[16:23], v[32:39], v[184:187]
	v_mfma_f32_16x16x128_f8f6f4 v[176:179], v[24:31], v[32:39], v[176:179]
	v_mfma_f32_16x16x128_f8f6f4 v[168:171], v[16:23], v[40:47], v[168:171]
	v_mfma_f32_16x16x128_f8f6f4 v[160:163], v[24:31], v[40:47], v[160:163]
	v_mfma_f32_16x16x128_f8f6f4 v[152:155], v[16:23], v[48:55], v[152:155]
	v_mfma_f32_16x16x128_f8f6f4 v[144:147], v[24:31], v[48:55], v[144:147]
	v_mfma_f32_16x16x128_f8f6f4 v[136:139], v[16:23], v[56:63], v[136:139]
	v_mfma_f32_16x16x128_f8f6f4 v[128:131], v[24:31], v[56:63], v[128:131]
	s_setprio 0
	s_barrier
	s_add_i32 s12, s14, s30
	v_lshl_add_u64 v[196:197], v[196:197], 0, s[62:63]
	s_mov_b32 m0, s12
	ds_read_b128 v[32:35], v238 offset:49152
	ds_read_b128 v[36:39], v238 offset:50176
	ds_read_b128 v[40:43], v238 offset:51200
	ds_read_b128 v[44:47], v238 offset:52224
	ds_read_b128 v[48:51], v238 offset:53248
	ds_read_b128 v[52:55], v238 offset:54272
	ds_read_b128 v[56:59], v238 offset:55296
	ds_read_b128 v[60:63], v238 offset:56320
	global_load_lds_dwordx4 v[196:197], off
	v_lshl_add_u64 v[196:197], v[198:199], 0, s[62:63]
	s_add_i32 m0, s12, 0x2000
	s_add_i32 s12, s15, s30
	global_load_lds_dwordx4 v[196:197], off
	v_lshl_add_u64 v[196:197], v[200:201], 0, s[62:63]
	s_mov_b32 m0, s12
	s_nop 0
	global_load_lds_dwordx4 v[196:197], off
	v_lshl_add_u64 v[196:197], v[202:203], 0, s[62:63]
	s_add_i32 m0, s12, 0x2000
	s_nop 0
	global_load_lds_dwordx4 v[196:197], off
	v_lshl_add_u64 v[196:197], v[226:227], 0, s[62:63]
	s_mov_b32 m0, s58
	s_nop 0
	global_load_lds_dwordx4 v[196:197], off
	v_lshl_add_u64 v[196:197], v[228:229], 0, s[62:63]
	s_mov_b32 m0, s59
	s_nop 0
	global_load_lds_dwordx4 v[196:197], off
	s_waitcnt vmcnt(8)
	s_waitcnt lgkmcnt(0)
	s_barrier
	s_setprio 1
	s_waitcnt lgkmcnt(0)
	v_mfma_f32_16x16x128_f8f6f4 v[124:127], v[0:7], v[32:39], v[124:127]
	v_mfma_f32_16x16x128_f8f6f4 v[116:119], v[8:15], v[32:39], v[116:119]
	v_mfma_f32_16x16x128_f8f6f4 v[108:111], v[0:7], v[40:47], v[108:111]
	v_mfma_f32_16x16x128_f8f6f4 v[100:103], v[8:15], v[40:47], v[100:103]
	v_mfma_f32_16x16x128_f8f6f4 v[92:95], v[0:7], v[48:55], v[92:95]
	v_mfma_f32_16x16x128_f8f6f4 v[84:87], v[8:15], v[48:55], v[84:87]
	v_mfma_f32_16x16x128_f8f6f4 v[76:79], v[0:7], v[56:63], v[76:79]
	v_mfma_f32_16x16x128_f8f6f4 v[68:71], v[8:15], v[56:63], v[68:71]
	s_setprio 0
	s_setprio 1
	v_mfma_f32_16x16x128_f8f6f4 v[120:123], v[16:23], v[32:39], v[120:123]
	v_mfma_f32_16x16x128_f8f6f4 v[112:115], v[24:31], v[32:39], v[112:115]
	v_mfma_f32_16x16x128_f8f6f4 v[104:107], v[16:23], v[40:47], v[104:107]
	v_mfma_f32_16x16x128_f8f6f4 v[96:99], v[24:31], v[40:47], v[96:99]
	v_mfma_f32_16x16x128_f8f6f4 v[88:91], v[16:23], v[48:55], v[88:91]
	v_mfma_f32_16x16x128_f8f6f4 v[80:83], v[24:31], v[48:55], v[80:83]
	v_mfma_f32_16x16x128_f8f6f4 v[72:75], v[16:23], v[56:63], v[72:75]
	v_mfma_f32_16x16x128_f8f6f4 v[64:67], v[24:31], v[56:63], v[64:67]
	s_setprio 0
	s_barrier
	s_add_i32 s83, s83, 2
	s_add_u32 s10, s10, 0x100
	s_addc_u32 s11, s11, 0
	s_add_u32 s49, s49, 0x100
	s_addc_u32 s82, s82, 0
	s_cmp_gt_u32 s83, 13
	s_cbranch_scc1 .LBB0_1083

; __device__ __forceinline__ unsigned pk4_fp8(float a, float b, float c, float d) { int w = __builtin_amdgcn_cvt_pk_fp8_f32(a, b, 0, false); w = __builtin_amdgcn_cvt_pk_fp8_f32(c, d, w, true); return (unsigned)w; }
; __device__ __forceinline__ float sigmoidf_(float x) { return __builtin_amdgcn_rcpf(1.0f + __expf(-x)); }
; __device__ __forceinline__ unsigned cvt_pk_bf16(float lo, float hi) { typedef __bf16 bf16x2_t __attribute__((ext_vector_type(2))); f32x2 v = {lo, hi}; bf16x2_t b = __builtin_convertvector(v, bf16x2_t); return __builtin_bit_cast(unsigned, b); }
;     __device__ __forceinline__ void operator()(const f32x4 (&acc)[2][2][4][2], const Unit& u, int wr, int wc, int fr, int fq) const {
;         const int row0 = u.pm * BM + wr * 64 + fr, col0 = u.pn * HALF + wc * 32 + 8 * fq;
; #pragma unroll
;         for (int ai = 0; ai < 2; ++ai)
; #pragma unroll
;             for (int m = 0; m < 4; ++m) { const size_t off = (size_t)(row0 + ai * HALF + m * 16) * DEXP + col0;
;                 float hv[8];
; #pragma unroll
;                 for (int n = 0; n < 2; ++n)
; #pragma unroll
;                     for (int j = 0; j < 4; ++j) { const float gg = acc[ai][0][m][n][j] * isc, uu = acc[ai][1][m][n][j] * isc; hv[4 * n + j] = gg * sigmoidf_(gg) * uu; }
;                 if constexpr (FP8OUT) { u32x2 w; w.x = pk4_fp8(hv[0], hv[1], hv[2], hv[3]); w.y = pk4_fp8(hv[4], hv[5], hv[6], hv[7]); *(u32x2*)((unsigned char*)H + off) = w; }
;                 else { u32x4 w; w.x = cvt_pk_bf16(hv[0], hv[1]); w.y = cvt_pk_bf16(hv[2], hv[3]); w.z = cvt_pk_bf16(hv[4], hv[5]); w.w = cvt_pk_bf16(hv[6], hv[7]); *(u32x4*)((bf16*)H + off) = w; } }
.LBB0_1085:
	v_lshl_add_u32 v10, s79, 8, v235
	v_ashrrev_i32_e32 v11, 31, v10
	v_lshl_add_u32 v14, s8, 7, v237
	v_ashrrev_i32_e32 v15, 31, v14
	s_mov_b64 s[8:9], -1
	v_lshlrev_b64 v[10:11], 9, v[10:11]
	v_lshl_add_u64 v[10:11], s[42:43], 0, v[10:11]
	v_lshl_add_u64 v[10:11], v[10:11], 0, v[14:15]
	v_mov_b32_e32 v244, 0x3d000000
	v_pk_mul_f32 v[190:191], v[190:191], v[244:245] op_sel_hi:[1,0]
	v_pk_mul_f32 v[188:189], v[188:189], v[244:245] op_sel_hi:[1,0]
	v_pk_mul_f32 v[186:187], v[186:187], v[244:245] op_sel_hi:[1,0]
	v_pk_mul_f32 v[184:185], v[184:185], v[244:245] op_sel_hi:[1,0]
	v_pk_mul_f32 v[182:183], v[182:183], v[244:245] op_sel_hi:[1,0]
	v_pk_mul_f32 v[180:181], v[180:181], v[244:245] op_sel_hi:[1,0]
	v_pk_mul_f32 v[178:179], v[178:179], v[244:245] op_sel_hi:[1,0]
	v_pk_mul_f32 v[176:177], v[176:177], v[244:245] op_sel_hi:[1,0]
	v_pk_mul_f32 v[174:175], v[174:175], v[244:245] op_sel_hi:[1,0]
	v_pk_mul_f32 v[172:173], v[172:173], v[244:245] op_sel_hi:[1,0]
	v_pk_mul_f32 v[170:171], v[170:171], v[244:245] op_sel_hi:[1,0]
	v_pk_mul_f32 v[168:169], v[168:169], v[244:245] op_sel_hi:[1,0]
	v_pk_mul_f32 v[166:167], v[166:167], v[244:245] op_sel_hi:[1,0]
	v_pk_mul_f32 v[164:165], v[164:165], v[244:245] op_sel_hi:[1,0]
	v_pk_mul_f32 v[162:163], v[162:163], v[244:245] op_sel_hi:[1,0]
	v_pk_mul_f32 v[160:161], v[160:161], v[244:245] op_sel_hi:[1,0]
	v_pk_mul_f32 v[158:159], v[158:159], v[244:245] op_sel_hi:[1,0]
	v_pk_mul_f32 v[156:157], v[156:157], v[244:245] op_sel_hi:[1,0]
	v_pk_mul_f32 v[154:155], v[154:155], v[244:245] op_sel_hi:[1,0]
	v_pk_mul_f32 v[152:153], v[152:153], v[244:245] op_sel_hi:[1,0]
	v_pk_mul_f32 v[150:151], v[150:151], v[244:245] op_sel_hi:[1,0]
	v_pk_mul_f32 v[148:149], v[148:149], v[244:245] op_sel_hi:[1,0]
	v_pk_mul_f32 v[146:147], v[146:147], v[244:245] op_sel_hi:[1,0]
	v_pk_mul_f32 v[144:145], v[144:145], v[244:245] op_sel_hi:[1,0]
	v_pk_mul_f32 v[142:143], v[142:143], v[244:245] op_sel_hi:[1,0]
	v_pk_mul_f32 v[140:141], v[140:141], v[244:245] op_sel_hi:[1,0]
	v_pk_mul_f32 v[138:139], v[138:139], v[244:245] op_sel_hi:[1,0]
	v_pk_mul_f32 v[136:137], v[136:137], v[244:245] op_sel_hi:[1,0]
	v_pk_mul_f32 v[134:135], v[134:135], v[244:245] op_sel_hi:[1,0]
	v_pk_mul_f32 v[132:133], v[132:133], v[244:245] op_sel_hi:[1,0]
	v_pk_mul_f32 v[130:131], v[130:131], v[244:245] op_sel_hi:[1,0]
	v_pk_mul_f32 v[128:129], v[128:129], v[244:245] op_sel_hi:[1,0]
	v_pk_mul_f32 v[126:127], v[126:127], v[244:245] op_sel_hi:[1,0]
	v_pk_mul_f32 v[124:125], v[124:125], v[244:245] op_sel_hi:[1,0]
	v_pk_mul_f32 v[122:123], v[122:123], v[244:245] op_sel_hi:[1,0]
	v_pk_mul_f32 v[120:121], v[120:121], v[244:245] op_sel_hi:[1,0]
	v_pk_mul_f32 v[118:119], v[118:119], v[244:245] op_sel_hi:[1,0]
	v_pk_mul_f32 v[116:117], v[116:117], v[244:245] op_sel_hi:[1,0]
	v_pk_mul_f32 v[114:115], v[114:115], v[244:245] op_sel_hi:[1,0]
	v_pk_mul_f32 v[112:113], v[112:113], v[244:245] op_sel_hi:[1,0]
	v_pk_mul_f32 v[110:111], v[110:111], v[244:245] op_sel_hi:[1,0]
	v_pk_mul_f32 v[108:109], v[108:109], v[244:245] op_sel_hi:[1,0]
	v_pk_mul_f32 v[106:107], v[106:107], v[244:245] op_sel_hi:[1,0]
	v_pk_mul_f32 v[104:105], v[104:105], v[244:245] op_sel_hi:[1,0]
	v_pk_mul_f32 v[102:103], v[102:103], v[244:245] op_sel_hi:[1,0]
	v_pk_mul_f32 v[100:101], v[100:101], v[244:245] op_sel_hi:[1,0]
	v_pk_mul_f32 v[98:99], v[98:99], v[244:245] op_sel_hi:[1,0]
	v_pk_mul_f32 v[96:97], v[96:97], v[244:245] op_sel_hi:[1,0]
	v_pk_mul_f32 v[94:95], v[94:95], v[244:245] op_sel_hi:[1,0]
	v_pk_mul_f32 v[92:93], v[92:93], v[244:245] op_sel_hi:[1,0]
	v_pk_mul_f32 v[90:91], v[90:91], v[244:245] op_sel_hi:[1,0]
	v_pk_mul_f32 v[88:89], v[88:89], v[244:245] op_sel_hi:[1,0]
	v_pk_mul_f32 v[86:87], v[86:87], v[244:245] op_sel_hi:[1,0]
	v_pk_mul_f32 v[84:85], v[84:85], v[244:245] op_sel_hi:[1,0]
	v_pk_mul_f32 v[82:83], v[82:83], v[244:245] op_sel_hi:[1,0]
	v_pk_mul_f32 v[80:81], v[80:81], v[244:245] op_sel_hi:[1,0]
	v_pk_mul_f32 v[78:79], v[78:79], v[244:245] op_sel_hi:[1,0]
	v_pk_mul_f32 v[76:77], v[76:77], v[244:245] op_sel_hi:[1,0]
	v_pk_mul_f32 v[74:75], v[74:75], v[244:245] op_sel_hi:[1,0]
	v_pk_mul_f32 v[72:73], v[72:73], v[244:245] op_sel_hi:[1,0]
	v_pk_mul_f32 v[70:71], v[70:71], v[244:245] op_sel_hi:[1,0]
	v_pk_mul_f32 v[68:69], v[68:69], v[244:245] op_sel_hi:[1,0]
	v_pk_mul_f32 v[66:67], v[66:67], v[244:245] op_sel_hi:[1,0]
	v_pk_mul_f32 v[64:65], v[64:65], v[244:245] op_sel_hi:[1,0]
	v_mul_f32_e32 v0, 0xbfb8aa3b, v188
	v_mul_f32_e32 v1, 0xbfb8aa3b, v189
	v_mul_f32_e32 v2, 0xbfb8aa3b, v190
	v_mul_f32_e32 v3, 0xbfb8aa3b, v191
	v_mul_f32_e32 v4, 0xbfb8aa3b, v180
	v_mul_f32_e32 v5, 0xbfb8aa3b, v181
	v_mul_f32_e32 v6, 0xbfb8aa3b, v182
	v_mul_f32_e32 v7, 0xbfb8aa3b, v183
	v_exp_f32_e32 v0, v0
	v_exp_f32_e32 v1, v1
	v_exp_f32_e32 v2, v2
	v_exp_f32_e32 v3, v3
	v_exp_f32_e32 v4, v4
	v_exp_f32_e32 v5, v5
	v_exp_f32_e32 v6, v6
	v_exp_f32_e32 v7, v7
	v_add_f32_e32 v0, 1.0, v0
	v_add_f32_e32 v1, 1.0, v1
	v_add_f32_e32 v2, 1.0, v2
	v_add_f32_e32 v3, 1.0, v3
	v_add_f32_e32 v4, 1.0, v4
	v_add_f32_e32 v5, 1.0, v5
	v_add_f32_e32 v6, 1.0, v6
	v_add_f32_e32 v7, 1.0, v7
	v_rcp_f32_e32 v0, v0
	v_rcp_f32_e32 v1, v1
	v_rcp_f32_e32 v2, v2
	v_rcp_f32_e32 v3, v3
	v_rcp_f32_e32 v4, v4
	v_rcp_f32_e32 v5, v5
	v_rcp_f32_e32 v6, v6
	v_rcp_f32_e32 v7, v7
	v_mul_f32_e32 v0, v188, v0
	v_mul_f32_e32 v1, v189, v1
	v_mul_f32_e32 v2, v190, v2
	v_mul_f32_e32 v3, v191, v3
	v_mul_f32_e32 v4, v180, v4
	v_mul_f32_e32 v5, v181, v5
	v_mul_f32_e32 v6, v182, v6
	v_mul_f32_e32 v7, v183, v7
	v_mul_f32_e32 v0, v0, v184
	v_mul_f32_e32 v1, v1, v185
	v_mul_f32_e32 v2, v2, v186
	v_mul_f32_e32 v3, v3, v187
	v_mul_f32_e32 v4, v4, v176
; __device__ __forceinline__ unsigned pk4_fp8(float a, float b, float c, float d) { int w = __builtin_amdgcn_cvt_pk_fp8_f32(a, b, 0, false); w = __builtin_amdgcn_cvt_pk_fp8_f32(c, d, w, true); return (unsigned)w; }
; __device__ __forceinline__ float sigmoidf_(float x) { return __builtin_amdgcn_rcpf(1.0f + __expf(-x)); }
; __device__ __forceinline__ unsigned cvt_pk_bf16(float lo, float hi) { typedef __bf16 bf16x2_t __attribute__((ext_vector_type(2))); f32x2 v = {lo, hi}; bf16x2_t b = __builtin_convertvector(v, bf16x2_t); return __builtin_bit_cast(unsigned, b); }
;     __device__ __forceinline__ void operator()(const f32x4 (&acc)[2][2][4][2], const Unit& u, int wr, int wc, int fr, int fq) const {
;     ...
;             for (int m = 0; m < 4; ++m) { const size_t off = (size_t)(row0 + ai * HALF + m * 16) * DEXP + col0;
;                 float hv[8];
; #pragma unroll
;                 for (int n = 0; n < 2; ++n)
; #pragma unroll
;                     for (int j = 0; j < 4; ++j) { const float gg = acc[ai][0][m][n][j] * isc, uu = acc[ai][1][m][n][j] * isc; hv[4 * n + j] = gg * sigmoidf_(gg) * uu; }
;                 if constexpr (FP8OUT) { u32x2 w; w.x = pk4_fp8(hv[0], hv[1], hv[2], hv[3]); w.y = pk4_fp8(hv[4], hv[5], hv[6], hv[7]); *(u32x2*)((unsigned char*)H + off) = w; }
;                 else { u32x4 w; w.x = cvt_pk_bf16(hv[0], hv[1]); w.y = cvt_pk_bf16(hv[2], hv[3]); w.z = cvt_pk_bf16(hv[4], hv[5]); w.w = cvt_pk_bf16(hv[6], hv[7]); *(u32x4*)((bf16*)H + off) = w; } }
	v_mul_f32_e32 v5, v5, v177
	v_mul_f32_e32 v6, v6, v178
	v_mul_f32_e32 v7, v7, v179
	v_cvt_pk_fp8_f32 v8, v0, v1
	v_cvt_pk_fp8_f32 v9, v4, v5
	v_cvt_pk_fp8_f32 v8, v2, v3 op_sel:[0,0,1]
	v_cvt_pk_fp8_f32 v9, v6, v7 op_sel:[0,0,1]
	global_store_dwordx2 v[10:11], v[8:9], off
	v_mul_f32_e32 v16, 0xbfb8aa3b, v172
	v_mul_f32_e32 v17, 0xbfb8aa3b, v173
	v_mul_f32_e32 v18, 0xbfb8aa3b, v174
	v_mul_f32_e32 v19, 0xbfb8aa3b, v175
	v_mul_f32_e32 v20, 0xbfb8aa3b, v164
	v_mul_f32_e32 v21, 0xbfb8aa3b, v165
	v_mul_f32_e32 v22, 0xbfb8aa3b, v166
	v_mul_f32_e32 v23, 0xbfb8aa3b, v167
	v_add_co_u32_e32 v28, vcc, 0x2000, v10
	v_exp_f32_e32 v16, v16
	v_exp_f32_e32 v17, v17
	v_exp_f32_e32 v18, v18
	v_exp_f32_e32 v19, v19
	v_exp_f32_e32 v20, v20
	v_exp_f32_e32 v21, v21
	v_exp_f32_e32 v22, v22
	v_exp_f32_e32 v23, v23
	v_addc_co_u32_e32 v29, vcc, 0, v11, vcc
	v_add_f32_e32 v16, 1.0, v16
	v_add_f32_e32 v17, 1.0, v17
	v_add_f32_e32 v18, 1.0, v18
	v_add_f32_e32 v19, 1.0, v19
	v_add_f32_e32 v20, 1.0, v20
	v_add_f32_e32 v21, 1.0, v21
	v_add_f32_e32 v22, 1.0, v22
	v_add_f32_e32 v23, 1.0, v23
	v_rcp_f32_e32 v16, v16
	v_rcp_f32_e32 v17, v17
	v_rcp_f32_e32 v18, v18
	v_rcp_f32_e32 v19, v19
	v_rcp_f32_e32 v20, v20
	v_rcp_f32_e32 v21, v21
	v_rcp_f32_e32 v22, v22
	v_rcp_f32_e32 v23, v23
	v_mul_f32_e32 v16, v172, v16
	v_mul_f32_e32 v17, v173, v17
	v_mul_f32_e32 v18, v174, v18
	v_mul_f32_e32 v19, v175, v19
	v_mul_f32_e32 v20, v164, v20
	v_mul_f32_e32 v21, v165, v21
	v_mul_f32_e32 v22, v166, v22
	v_mul_f32_e32 v23, v167, v23
	v_mul_f32_e32 v16, v16, v168
	v_mul_f32_e32 v17, v17, v169
	v_mul_f32_e32 v18, v18, v170
	v_mul_f32_e32 v19, v19, v171
	v_mul_f32_e32 v20, v20, v160
	v_mul_f32_e32 v21, v21, v161
	v_mul_f32_e32 v22, v22, v162
	v_mul_f32_e32 v23, v23, v163
	v_cvt_pk_fp8_f32 v24, v16, v17
	v_cvt_pk_fp8_f32 v25, v20, v21
	v_cvt_pk_fp8_f32 v24, v18, v19 op_sel:[0,0,1]
	v_cvt_pk_fp8_f32 v25, v22, v23 op_sel:[0,0,1]
	global_store_dwordx2 v[28:29], v[24:25], off
	v_mul_f32_e32 v0, 0xbfb8aa3b, v156
	v_mul_f32_e32 v1, 0xbfb8aa3b, v157
	v_mul_f32_e32 v2, 0xbfb8aa3b, v158
	v_mul_f32_e32 v3, 0xbfb8aa3b, v159
	v_mul_f32_e32 v4, 0xbfb8aa3b, v148
	v_mul_f32_e32 v5, 0xbfb8aa3b, v149
	v_mul_f32_e32 v6, 0xbfb8aa3b, v150
	v_mul_f32_e32 v7, 0xbfb8aa3b, v151
	v_add_co_u32_e32 v12, vcc, 0x4000, v10
	v_exp_f32_e32 v0, v0
	v_exp_f32_e32 v1, v1
	v_exp_f32_e32 v2, v2
	v_exp_f32_e32 v3, v3
	v_exp_f32_e32 v4, v4
	v_exp_f32_e32 v5, v5
	v_exp_f32_e32 v6, v6
	v_exp_f32_e32 v7, v7
	v_addc_co_u32_e32 v13, vcc, 0, v11, vcc
	v_add_f32_e32 v0, 1.0, v0
	v_add_f32_e32 v1, 1.0, v1
	v_add_f32_e32 v2, 1.0, v2
	v_add_f32_e32 v3, 1.0, v3
	v_add_f32_e32 v4, 1.0, v4
	v_add_f32_e32 v5, 1.0, v5
	v_add_f32_e32 v6, 1.0, v6
	v_add_f32_e32 v7, 1.0, v7
	v_rcp_f32_e32 v0, v0
	v_rcp_f32_e32 v1, v1
	v_rcp_f32_e32 v2, v2
	v_rcp_f32_e32 v3, v3
	v_rcp_f32_e32 v4, v4
	v_rcp_f32_e32 v5, v5
	v_rcp_f32_e32 v6, v6
	v_rcp_f32_e32 v7, v7
	v_mul_f32_e32 v0, v156, v0
	v_mul_f32_e32 v1, v157, v1
	v_mul_f32_e32 v2, v158, v2
	v_mul_f32_e32 v3, v159, v3
	v_mul_f32_e32 v4, v148, v4
	v_mul_f32_e32 v5, v149, v5
	v_mul_f32_e32 v6, v150, v6
	v_mul_f32_e32 v7, v151, v7
	v_mul_f32_e32 v0, v0, v152
	v_mul_f32_e32 v1, v1, v153
	v_mul_f32_e32 v2, v2, v154
	v_mul_f32_e32 v3, v3, v155
	v_mul_f32_e32 v4, v4, v144
	v_mul_f32_e32 v5, v5, v145
	v_mul_f32_e32 v6, v6, v146
	v_mul_f32_e32 v7, v7, v147
	v_cvt_pk_fp8_f32 v8, v0, v1
	v_cvt_pk_fp8_f32 v9, v4, v5
	v_cvt_pk_fp8_f32 v8, v2, v3 op_sel:[0,0,1]
	v_cvt_pk_fp8_f32 v9, v6, v7 op_sel:[0,0,1]
	global_store_dwordx2 v[12:13], v[8:9], off
	v_mul_f32_e32 v16, 0xbfb8aa3b, v140
	v_mul_f32_e32 v17, 0xbfb8aa3b, v141
	v_mul_f32_e32 v18, 0xbfb8aa3b, v142
	v_mul_f32_e32 v19, 0xbfb8aa3b, v143
	v_mul_f32_e32 v20, 0xbfb8aa3b, v132
	v_mul_f32_e32 v21, 0xbfb8aa3b, v133
	v_mul_f32_e32 v22, 0xbfb8aa3b, v134
	v_mul_f32_e32 v23, 0xbfb8aa3b, v135
	v_add_co_u32_e32 v28, vcc, 0x6000, v10
	v_exp_f32_e32 v16, v16
	v_exp_f32_e32 v17, v17
	v_exp_f32_e32 v18, v18
	v_exp_f32_e32 v19, v19
	v_exp_f32_e32 v20, v20
	v_exp_f32_e32 v21, v21
	v_exp_f32_e32 v22, v22
	v_exp_f32_e32 v23, v23
	v_addc_co_u32_e32 v29, vcc, 0, v11, vcc
	v_add_f32_e32 v16, 1.0, v16
	v_add_f32_e32 v17, 1.0, v17
	v_add_f32_e32 v18, 1.0, v18
	v_add_f32_e32 v19, 1.0, v19
	v_add_f32_e32 v20, 1.0, v20
	v_add_f32_e32 v21, 1.0, v21
	v_add_f32_e32 v22, 1.0, v22
	v_add_f32_e32 v23, 1.0, v23
	v_rcp_f32_e32 v16, v16
	v_rcp_f32_e32 v17, v17
	v_rcp_f32_e32 v18, v18
	v_rcp_f32_e32 v19, v19
	v_rcp_f32_e32 v20, v20
	v_rcp_f32_e32 v21, v21
	v_rcp_f32_e32 v22, v22
	v_rcp_f32_e32 v23, v23
	v_mul_f32_e32 v16, v140, v16
	v_mul_f32_e32 v17, v141, v17
	v_mul_f32_e32 v18, v142, v18
	v_mul_f32_e32 v19, v143, v19
	v_mul_f32_e32 v20, v132, v20
	v_mul_f32_e32 v21, v133, v21
	v_mul_f32_e32 v22, v134, v22
	v_mul_f32_e32 v23, v135, v23
	v_mul_f32_e32 v16, v16, v136
	v_mul_f32_e32 v17, v17, v137
	v_mul_f32_e32 v18, v18, v138
	v_mul_f32_e32 v19, v19, v139
	v_mul_f32_e32 v20, v20, v128
	v_mul_f32_e32 v21, v21, v129
	v_mul_f32_e32 v22, v22, v130
	v_mul_f32_e32 v23, v23, v131
	v_cvt_pk_fp8_f32 v24, v16, v17
	v_cvt_pk_fp8_f32 v25, v20, v21
	v_cvt_pk_fp8_f32 v24, v18, v19 op_sel:[0,0,1]
	v_cvt_pk_fp8_f32 v25, v22, v23 op_sel:[0,0,1]
	global_store_dwordx2 v[28:29], v[24:25], off
	v_mul_f32_e32 v0, 0xbfb8aa3b, v124
	v_mul_f32_e32 v1, 0xbfb8aa3b, v125
	v_mul_f32_e32 v2, 0xbfb8aa3b, v126
	v_mul_f32_e32 v3, 0xbfb8aa3b, v127
	v_mul_f32_e32 v4, 0xbfb8aa3b, v116
	v_mul_f32_e32 v5, 0xbfb8aa3b, v117
	v_mul_f32_e32 v6, 0xbfb8aa3b, v118
	v_mul_f32_e32 v7, 0xbfb8aa3b, v119
	v_add_co_u32_e32 v12, vcc, 0x10000, v10
	v_exp_f32_e32 v0, v0
	v_exp_f32_e32 v1, v1
	v_exp_f32_e32 v2, v2
	v_exp_f32_e32 v3, v3
	v_exp_f32_e32 v4, v4
; __device__ __forceinline__ unsigned pk4_fp8(float a, float b, float c, float d) { int w = __builtin_amdgcn_cvt_pk_fp8_f32(a, b, 0, false); w = __builtin_amdgcn_cvt_pk_fp8_f32(c, d, w, true); return (unsigned)w; }
; __device__ __forceinline__ float sigmoidf_(float x) { return __builtin_amdgcn_rcpf(1.0f + __expf(-x)); }
; #define PG8_BAR __builtin_amdgcn_s_barrier()
; __device__ __forceinline__ unsigned cvt_pk_bf16(float lo, float hi) { typedef __bf16 bf16x2_t __attribute__((ext_vector_type(2))); f32x2 v = {lo, hi}; bf16x2_t b = __builtin_convertvector(v, bf16x2_t); return __builtin_bit_cast(unsigned, b); }
; template <class Epi, class Sched, bool GATHER, bool FP8 = false, bool ALIGN = true>
; __device__ __forceinline__ void gemm_phase(LAS unsigned char* lds, int wave, const Gemm g, const Sched& S, const Epi& E) {
;     ...
;         if (!has_next) break;
; #pragma unroll
;         for (int a = 0; a < 2; ++a)
; #pragma unroll
;             for (int b = 0; b < 2; ++b)
; #pragma unroll
;                 for (int m = 0; m < 4; ++m)
; #pragma unroll
;                     for (int n = 0; n < 2; ++n) acc[a][b][m][n] = (f32x4){0.f, 0.f, 0.f, 0.f};
;         cur = nxt; cB = nB; ++ui;
;         if constexpr (ALIGN) { if (wr == 1) PG8_BAR; }
;     __device__ __forceinline__ void operator()(const f32x4 (&acc)[2][2][4][2], const Unit& u, int wr, int wc, int fr, int fq) const {
;     ...
;             for (int m = 0; m < 4; ++m) { const size_t off = (size_t)(row0 + ai * HALF + m * 16) * DEXP + col0;
;                 float hv[8];
; #pragma unroll
;                 for (int n = 0; n < 2; ++n)
; #pragma unroll
;                     for (int j = 0; j < 4; ++j) { const float gg = acc[ai][0][m][n][j] * isc, uu = acc[ai][1][m][n][j] * isc; hv[4 * n + j] = gg * sigmoidf_(gg) * uu; }
;                 if constexpr (FP8OUT) { u32x2 w; w.x = pk4_fp8(hv[0], hv[1], hv[2], hv[3]); w.y = pk4_fp8(hv[4], hv[5], hv[6], hv[7]); *(u32x2*)((unsigned char*)H + off) = w; }
;                 else { u32x4 w; w.x = cvt_pk_bf16(hv[0], hv[1]); w.y = cvt_pk_bf16(hv[2], hv[3]); w.z = cvt_pk_bf16(hv[4], hv[5]); w.w = cvt_pk_bf16(hv[6], hv[7]); *(u32x4*)((bf16*)H + off) = w; } }
	v_exp_f32_e32 v5, v5
	v_exp_f32_e32 v6, v6
	v_exp_f32_e32 v7, v7
	v_addc_co_u32_e32 v13, vcc, 0, v11, vcc
	v_add_f32_e32 v0, 1.0, v0
	v_add_f32_e32 v1, 1.0, v1
	v_add_f32_e32 v2, 1.0, v2
	v_add_f32_e32 v3, 1.0, v3
	v_add_f32_e32 v4, 1.0, v4
	v_add_f32_e32 v5, 1.0, v5
	v_add_f32_e32 v6, 1.0, v6
	v_add_f32_e32 v7, 1.0, v7
	v_rcp_f32_e32 v0, v0
	v_rcp_f32_e32 v1, v1
	v_rcp_f32_e32 v2, v2
	v_rcp_f32_e32 v3, v3
	v_rcp_f32_e32 v4, v4
	v_rcp_f32_e32 v5, v5
	v_rcp_f32_e32 v6, v6
	v_rcp_f32_e32 v7, v7
	v_mul_f32_e32 v0, v124, v0
	v_mul_f32_e32 v1, v125, v1
	v_mul_f32_e32 v2, v126, v2
	v_mul_f32_e32 v3, v127, v3
	v_mul_f32_e32 v4, v116, v4
	v_mul_f32_e32 v5, v117, v5
	v_mul_f32_e32 v6, v118, v6
	v_mul_f32_e32 v7, v119, v7
	v_mul_f32_e32 v0, v0, v120
	v_mul_f32_e32 v1, v1, v121
	v_mul_f32_e32 v2, v2, v122
	v_mul_f32_e32 v3, v3, v123
	v_mul_f32_e32 v4, v4, v112
	v_mul_f32_e32 v5, v5, v113
	v_mul_f32_e32 v6, v6, v114
	v_mul_f32_e32 v7, v7, v115
	v_cvt_pk_fp8_f32 v8, v0, v1
	v_cvt_pk_fp8_f32 v9, v4, v5
	v_cvt_pk_fp8_f32 v8, v2, v3 op_sel:[0,0,1]
	v_cvt_pk_fp8_f32 v9, v6, v7 op_sel:[0,0,1]
	global_store_dwordx2 v[12:13], v[8:9], off
	v_mul_f32_e32 v16, 0xbfb8aa3b, v108
	v_mul_f32_e32 v17, 0xbfb8aa3b, v109
	v_mul_f32_e32 v18, 0xbfb8aa3b, v110
	v_mul_f32_e32 v19, 0xbfb8aa3b, v111
	v_mul_f32_e32 v20, 0xbfb8aa3b, v100
	v_mul_f32_e32 v21, 0xbfb8aa3b, v101
	v_mul_f32_e32 v22, 0xbfb8aa3b, v102
	v_mul_f32_e32 v23, 0xbfb8aa3b, v103
	v_add_co_u32_e32 v28, vcc, 0x12000, v10
	v_exp_f32_e32 v16, v16
	v_exp_f32_e32 v17, v17
	v_exp_f32_e32 v18, v18
	v_exp_f32_e32 v19, v19
	v_exp_f32_e32 v20, v20
	v_exp_f32_e32 v21, v21
	v_exp_f32_e32 v22, v22
	v_exp_f32_e32 v23, v23
	v_addc_co_u32_e32 v29, vcc, 0, v11, vcc
	v_add_f32_e32 v16, 1.0, v16
	v_add_f32_e32 v17, 1.0, v17
	v_add_f32_e32 v18, 1.0, v18
	v_add_f32_e32 v19, 1.0, v19
	v_add_f32_e32 v20, 1.0, v20
	v_add_f32_e32 v21, 1.0, v21
	v_add_f32_e32 v22, 1.0, v22
	v_add_f32_e32 v23, 1.0, v23
	v_rcp_f32_e32 v16, v16
	v_rcp_f32_e32 v17, v17
	v_rcp_f32_e32 v18, v18
	v_rcp_f32_e32 v19, v19
	v_rcp_f32_e32 v20, v20
	v_rcp_f32_e32 v21, v21
	v_rcp_f32_e32 v22, v22
	v_rcp_f32_e32 v23, v23
	v_mul_f32_e32 v16, v108, v16
	v_mul_f32_e32 v17, v109, v17
	v_mul_f32_e32 v18, v110, v18
	v_mul_f32_e32 v19, v111, v19
	v_mul_f32_e32 v20, v100, v20
	v_mul_f32_e32 v21, v101, v21
	v_mul_f32_e32 v22, v102, v22
	v_mul_f32_e32 v23, v103, v23
	v_mul_f32_e32 v16, v16, v104
	v_mul_f32_e32 v17, v17, v105
	v_mul_f32_e32 v18, v18, v106
	v_mul_f32_e32 v19, v19, v107
	v_mul_f32_e32 v20, v20, v96
	v_mul_f32_e32 v21, v21, v97
	v_mul_f32_e32 v22, v22, v98
	v_mul_f32_e32 v23, v23, v99
	v_cvt_pk_fp8_f32 v24, v16, v17
	v_cvt_pk_fp8_f32 v25, v20, v21
	v_cvt_pk_fp8_f32 v24, v18, v19 op_sel:[0,0,1]
	v_cvt_pk_fp8_f32 v25, v22, v23 op_sel:[0,0,1]
	global_store_dwordx2 v[28:29], v[24:25], off
	v_mul_f32_e32 v0, 0xbfb8aa3b, v92
	v_mul_f32_e32 v1, 0xbfb8aa3b, v93
	v_mul_f32_e32 v2, 0xbfb8aa3b, v94
	v_mul_f32_e32 v3, 0xbfb8aa3b, v95
	v_mul_f32_e32 v4, 0xbfb8aa3b, v84
	v_mul_f32_e32 v5, 0xbfb8aa3b, v85
	v_mul_f32_e32 v6, 0xbfb8aa3b, v86
	v_mul_f32_e32 v7, 0xbfb8aa3b, v87
	v_add_co_u32_e32 v12, vcc, 0x14000, v10
	v_exp_f32_e32 v0, v0
	v_exp_f32_e32 v1, v1
	v_exp_f32_e32 v2, v2
	v_exp_f32_e32 v3, v3
	v_exp_f32_e32 v4, v4
	v_exp_f32_e32 v5, v5
	v_exp_f32_e32 v6, v6
	v_exp_f32_e32 v7, v7
	v_addc_co_u32_e32 v13, vcc, 0, v11, vcc
	v_add_f32_e32 v0, 1.0, v0
	v_add_f32_e32 v1, 1.0, v1
	v_add_f32_e32 v2, 1.0, v2
	v_add_f32_e32 v3, 1.0, v3
	v_add_f32_e32 v4, 1.0, v4
	v_add_f32_e32 v5, 1.0, v5
	v_add_f32_e32 v6, 1.0, v6
	v_add_f32_e32 v7, 1.0, v7
	v_rcp_f32_e32 v0, v0
	v_rcp_f32_e32 v1, v1
	v_rcp_f32_e32 v2, v2
	v_rcp_f32_e32 v3, v3
	v_rcp_f32_e32 v4, v4
	v_rcp_f32_e32 v5, v5
	v_rcp_f32_e32 v6, v6
	v_rcp_f32_e32 v7, v7
	v_mul_f32_e32 v0, v92, v0
	v_mul_f32_e32 v1, v93, v1
	v_mul_f32_e32 v2, v94, v2
	v_mul_f32_e32 v3, v95, v3
	v_mul_f32_e32 v4, v84, v4
	v_mul_f32_e32 v5, v85, v5
	v_mul_f32_e32 v6, v86, v6
	v_mul_f32_e32 v7, v87, v7
	v_mul_f32_e32 v0, v0, v88
	v_mul_f32_e32 v1, v1, v89
	v_mul_f32_e32 v2, v2, v90
	v_mul_f32_e32 v3, v3, v91
	v_mul_f32_e32 v4, v4, v80
	v_mul_f32_e32 v5, v5, v81
	v_mul_f32_e32 v6, v6, v82
	v_mul_f32_e32 v7, v7, v83
	v_cvt_pk_fp8_f32 v8, v0, v1
	v_cvt_pk_fp8_f32 v9, v4, v5
	v_cvt_pk_fp8_f32 v8, v2, v3 op_sel:[0,0,1]
	v_cvt_pk_fp8_f32 v9, v6, v7 op_sel:[0,0,1]
	global_store_dwordx2 v[12:13], v[8:9], off
	v_mul_f32_e32 v16, 0xbfb8aa3b, v76
	v_mul_f32_e32 v17, 0xbfb8aa3b, v77
	v_mul_f32_e32 v18, 0xbfb8aa3b, v78
	v_mul_f32_e32 v19, 0xbfb8aa3b, v79
	v_mul_f32_e32 v20, 0xbfb8aa3b, v68
	v_mul_f32_e32 v21, 0xbfb8aa3b, v69
	v_mul_f32_e32 v22, 0xbfb8aa3b, v70
	v_mul_f32_e32 v23, 0xbfb8aa3b, v71
	v_add_co_u32_e32 v28, vcc, 0x16000, v10
	v_exp_f32_e32 v16, v16
	v_exp_f32_e32 v17, v17
	v_exp_f32_e32 v18, v18
	v_exp_f32_e32 v19, v19
	v_exp_f32_e32 v20, v20
	v_exp_f32_e32 v21, v21
	v_exp_f32_e32 v22, v22
	v_exp_f32_e32 v23, v23
	v_addc_co_u32_e32 v29, vcc, 0, v11, vcc
	v_add_f32_e32 v16, 1.0, v16
	v_add_f32_e32 v17, 1.0, v17
	v_add_f32_e32 v18, 1.0, v18
	v_add_f32_e32 v19, 1.0, v19
	v_add_f32_e32 v20, 1.0, v20
	v_add_f32_e32 v21, 1.0, v21
	v_add_f32_e32 v22, 1.0, v22
	v_add_f32_e32 v23, 1.0, v23
	v_rcp_f32_e32 v16, v16
	v_rcp_f32_e32 v17, v17
	v_rcp_f32_e32 v18, v18
	v_rcp_f32_e32 v19, v19
	v_rcp_f32_e32 v20, v20
	v_rcp_f32_e32 v21, v21
	v_rcp_f32_e32 v22, v22
	v_rcp_f32_e32 v23, v23
	v_mul_f32_e32 v16, v76, v16
	v_mul_f32_e32 v17, v77, v17
	v_mul_f32_e32 v18, v78, v18
	v_mul_f32_e32 v19, v79, v19
	v_mul_f32_e32 v20, v68, v20
	v_mul_f32_e32 v21, v69, v21
	v_mul_f32_e32 v22, v70, v22
	v_mul_f32_e32 v23, v71, v23
	v_mul_f32_e32 v16, v16, v72
	v_mul_f32_e32 v17, v17, v73
	v_mul_f32_e32 v18, v18, v74
	v_mul_f32_e32 v19, v19, v75
	v_mul_f32_e32 v20, v20, v64
	v_mul_f32_e32 v21, v21, v65
	v_mul_f32_e32 v22, v22, v66
	v_mul_f32_e32 v23, v23, v67
	v_cvt_pk_fp8_f32 v24, v16, v17
	v_cvt_pk_fp8_f32 v25, v20, v21
	v_cvt_pk_fp8_f32 v24, v18, v19 op_sel:[0,0,1]
	v_cvt_pk_fp8_f32 v25, v22, v23 op_sel:[0,0,1]
	s_andn2_b64 vcc, exec, s[50:51]
	global_store_dwordx2 v[28:29], v[24:25], off
	s_cbranch_vccnz .LBB0_1073
	s_andn2_b64 vcc, exec, s[38:39]
	s_cbranch_vccnz .LBB0_1072
	s_barrier
	s_branch .LBB0_1072
